# speedup vs baseline: 1.0041x; 1.0041x over previous
_Z11lstm_kernelPKiPKhPKfS4_S4_Pf:
	s_load_dwordx4 s[12:15], s[0:1], 0x0
	v_readfirstlane_b32 s19, v0
	v_or_b32_e32 v3, 0x400, v0
	s_movk_i32 s4, 0x500
	s_lshr_b32 s7, s19, 6
	s_lshl_b32 s18, s2, 6
	s_mulk_i32 s2, 0x1400
	v_mov_b32_e32 v2, 0x4ff
	v_cmp_gt_u32_e32 vcc, s4, v3
	s_mul_hi_i32 s3, s18, 0x50
	s_waitcnt lgkmcnt(0)
	s_add_u32 s2, s12, s2
	v_cndmask_b32_e32 v2, v2, v3, vcc
	s_addc_u32 s3, s13, s3
	v_lshlrev_b32_e32 v1, 2, v0
	v_lshlrev_b32_e32 v4, 2, v2
	s_movk_i32 s4, 0x184
	v_or_b32_e32 v28, 0x200, v0
	global_load_dword v29, v1, s[2:3]
	global_load_dword v30, v1, s[2:3] offset:2048
	global_load_dword v2, v4, s[2:3]
	v_mov_b32_e32 v4, 0x383
	v_cmp_gt_u32_e32 vcc, s4, v0
	s_add_u32 s2, s14, 0x34000
	s_addc_u32 s3, s15, 0
	v_cndmask_b32_e32 v4, v4, v28, vcc
	v_lshlrev_b32_e32 v31, 4, v0
	v_lshlrev_b32_e32 v4, 4, v4
	global_load_dwordx4 v[6:9], v31, s[2:3]
	global_load_dwordx4 v[10:13], v4, s[2:3]
	v_and_b32_e32 v4, 0x7f, v0
	v_lshlrev_b32_e32 v18, 4, v4
	v_mov_b32_e32 v19, 0
	v_lshl_add_u64 v[4:5], s[14:15], 0, v[18:19]
	s_mov_b32 s2, 0x37000
	v_add_co_u32_e64 v4, s[2:3], s2, v4
	s_nop 1
	v_addc_co_u32_e64 v5, s[2:3], 0, v5, s[2:3]
	global_load_dwordx4 v[14:17], v[4:5], off offset:2112
	s_movk_i32 s22, 0x410
	s_movk_i32 s2, 0x4ff
	v_and_b32_e32 v4, 63, v0
	v_cmp_lt_u32_e64 s[2:3], s2, v3
	s_mul_i32 s5, s7, 0x6000
	s_mul_hi_u32 s4, s7, 0x6000
	s_add_u32 s8, s14, s5
	s_addc_u32 s9, s15, s4
	v_lshlrev_b32_e32 v210, 4, v4
	v_mov_b32_e32 v211, v19
	v_lshl_add_u64 v[20:21], s[8:9], 0, v[210:211]
	s_movk_i32 s4, 0x2000
	v_add_co_u32_e64 v22, s[4:5], s4, v20
	s_nop 1
	v_addc_co_u32_e64 v23, s[4:5], 0, v21, s[4:5]
	s_movk_i32 s4, 0x3000
	s_nop 0
	v_add_co_u32_e64 v24, s[4:5], s4, v20
	global_load_dwordx4 v[90:93], v[22:23], off offset:1024
	global_load_dwordx4 v[86:89], v[22:23], off offset:2048
	v_addc_co_u32_e64 v25, s[4:5], 0, v21, s[4:5]
	s_movk_i32 s4, 0x5000
	s_nop 0
	v_add_co_u32_e64 v26, s[4:5], s4, v20
	s_nop 1
	v_addc_co_u32_e64 v27, s[4:5], 0, v21, s[4:5]
	global_load_dwordx4 v[82:85], v[22:23], off offset:3072
	global_load_dwordx4 v[46:49], v[26:27], off
	global_load_dwordx4 v[42:45], v[26:27], off offset:1024
	global_load_dwordx4 v[38:41], v[26:27], off offset:2048
	global_load_dwordx4 v[94:97], v[24:25], off offset:-4096
	global_load_dwordx4 v[34:37], v[26:27], off offset:3072
	s_movk_i32 s4, 0x1000
	v_add_co_u32_e64 v22, s[4:5], s4, v20
	global_load_dwordx4 v[126:129], v210, s[8:9]
	global_load_dwordx4 v[122:125], v210, s[8:9] offset:1024
	global_load_dwordx4 v[118:121], v210, s[8:9] offset:2048
	global_load_dwordx4 v[114:117], v210, s[8:9] offset:3072
	v_addc_co_u32_e64 v23, s[4:5], 0, v21, s[4:5]
	global_load_dwordx4 v[110:113], v[22:23], off
	global_load_dwordx4 v[106:109], v[22:23], off offset:1024
	global_load_dwordx4 v[102:105], v[22:23], off offset:2048
	global_load_dwordx4 v[98:101], v[22:23], off offset:3072
	global_load_dwordx4 v[78:81], v[24:25], off
	global_load_dwordx4 v[74:77], v[24:25], off offset:1024
	global_load_dwordx4 v[70:73], v[24:25], off offset:2048
	global_load_dwordx4 v[66:69], v[24:25], off offset:3072
	s_movk_i32 s4, 0x4000
	v_add_co_u32_e64 v20, s[4:5], s4, v20
	v_mov_b32_e32 v5, 0x4000
	s_nop 0
	v_addc_co_u32_e64 v21, s[4:5], 0, v21, s[4:5]
	global_load_dwordx4 v[62:65], v[20:21], off
	global_load_dwordx4 v[58:61], v[20:21], off offset:1024
	global_load_dwordx4 v[54:57], v[20:21], off offset:2048
	global_load_dwordx4 v[50:53], v[20:21], off offset:3072
	s_waitcnt vmcnt(26)
	ds_write_b128 v31, v[6:9] offset:16384
	v_lshl_or_b32 v5, v28, 4, v5
	v_add_u32_e32 v6, 0x9840, v31
	v_cndmask_b32_e32 v5, v6, v5, vcc
	s_waitcnt vmcnt(25)
	ds_write_b128 v5, v[10:13]
	s_waitcnt vmcnt(24)
	ds_write_b128 v18, v[14:17] offset:36928
	v_mul_u32_u24_e32 v5, 0xccd, v0
	v_lshrrev_b32_e32 v5, 16, v5
	s_mov_b32 s5, 0xffffec
	v_mul_u32_u24_e32 v6, 0xccd, v28
	s_movk_i32 s4, 0x90
	v_mad_u32_u24 v8, v5, s5, v0
	v_lshlrev_b32_e32 v5, 2, v5
	v_lshrrev_b32_e32 v6, 16, v6
	v_mul_lo_u32 v7, v29, s4
	v_lshl_or_b32 v5, v8, 8, v5
	ds_write_b32 v5, v7 offset:30784
	v_mul_lo_u32 v196, v29, s22
	v_add_u32_e32 v197, 0x24e80, v5
	ds_write_b32 v197, v196
	v_mad_u32_u24 v7, v6, s5, v28
	v_lshlrev_b32_e32 v6, 2, v6
	v_mul_lo_u32 v5, v30, s4
	v_lshl_or_b32 v6, v7, 8, v6
	ds_write_b32 v6, v5 offset:30784
	v_mul_lo_u32 v198, v30, s22
	v_add_u32_e32 v199, 0x24e80, v6
	ds_write_b32 v199, v198
	s_and_saveexec_b64 s[4:5], s[2:3]
	s_xor_b64 s[2:3], exec, s[4:5]
	v_mov_b32_e32 v3, 0x9840
	v_lshl_add_u32 v5, v0, 2, v3
	s_andn2_saveexec_b64 s[2:3], s[2:3]
	v_mul_u32_u24_e32 v5, 0xccd, v3
	s_mov_b32 s4, 0xffffec
	v_mul_u32_u24_sdwa v6, v5, s4 dst_sel:DWORD dst_unused:UNUSED_PAD src0_sel:WORD_1 src1_sel:DWORD
	v_add_lshl_u32 v3, v6, v3, 8
	v_mov_b32_e32 v6, 2
	v_lshlrev_b32_sdwa v5, v6, v5 dst_sel:DWORD dst_unused:UNUSED_PAD src0_sel:DWORD src1_sel:WORD_1
	s_movk_i32 s4, 0x7840
	v_add3_u32 v5, v5, v3, s4
	s_or_b64 exec, exec, s[2:3]
	v_lshrrev_b32_e32 v3, 5, v4
	s_movk_i32 s2, 0x90
	s_lshl_b32 s6, s7, 10
	s_mulk_i32 s7, 0xfd00
	v_and_b32_e32 v182, 31, v0
	v_mul_lo_u32 v200, v2, s22
	v_mul_lo_u32 v2, v2, s2
	s_add_i32 s7, s6, s7
	v_lshlrev_b32_e32 v229, 6, v3
	ds_write_b32 v5, v2
	v_add_u32_e32 v201, 0x1d640, v5
	ds_write_b32 v201, v200
	v_lshlrev_b32_e32 v230, 4, v3
	v_lshlrev_b32_e32 v228, 2, v182
	v_or_b32_e32 v2, s7, v229
	s_waitcnt lgkmcnt(0)
	s_barrier
	s_cmpk_lt_u32 s19, 0x100
	s_cbranch_scc1 .Llight_path
	s_setprio 1
	s_mov_b32 s12, 0xbeb17218
	v_add_u32_e32 v3, 0x7800, v228
	ds_read2_b32 v[138:139], v3 offset0:16 offset1:48
	ds_read_b128 v[18:21], v2 offset:36928
	ds_read_b128 v[22:25], v2 offset:36944
	s_waitcnt lgkmcnt(2)
	v_add_u32_e32 v3, v230, v138
	ds_read_b128 v[26:29], v2 offset:36960
	ds_read_b128 v[30:33], v2 offset:36976
	ds_read_b128 v[142:145], v3 offset:16384
	ds_read_b128 v[130:133], v3 offset:16416
	ds_read_b128 v[154:157], v3 offset:16448
	ds_read_b128 v[134:137], v3 offset:16480
	ds_read_b128 v[248:251], v2 offset:37104
	ds_read_b128 v[244:247], v2 offset:37088
	ds_read_b128 v[240:243], v2 offset:37072
	ds_read_b128 v[236:239], v2 offset:37056
	s_waitcnt vmcnt(17) lgkmcnt(7)
	v_mfma_f32_32x32x16_bf16 v[18:33], v[94:97], v[142:145], v[18:33]
	s_waitcnt lgkmcnt(6)
	v_mfma_f32_32x32x16_bf16 v[18:33], v[90:93], v[130:133], v[18:33]
	s_waitcnt lgkmcnt(5)
	v_mfma_f32_32x32x16_bf16 v[18:33], v[86:89], v[154:157], v[18:33]
	s_waitcnt lgkmcnt(4)
	v_mfma_f32_32x32x16_bf16 v[18:33], v[82:85], v[134:137], v[18:33]
	s_cmpk_lt_u32 s19, 0x100
	s_cselect_b64 s[2:3], -1, 0
	ds_read_b32 v158, v228 offset:31040
	v_add_u32_e32 v159, v230, v139
	s_nop 2
	v_exp_f32_e32 v139, v20
	v_exp_f32_e32 v138, v24
	v_exp_f32_e32 v141, v28
	v_exp_f32_e32 v140, v32
	v_exp_f32_e32 v18, v18
	v_exp_f32_e32 v20, v22
	v_exp_f32_e32 v22, v26
	v_add_f32_e32 v24, 1.0, v138
	v_add_f32_e32 v26, 1.0, v141
	v_add_f32_e32 v19, 1.0, v139
	v_exp_f32_e32 v23, v30
	v_add_f32_e32 v27, 1.0, v140
	v_fmac_f32_e32 v24, v20, v24
	v_fmac_f32_e32 v26, v22, v26
	v_fmac_f32_e32 v19, v18, v19
	v_fmac_f32_e32 v27, v23, v27
	v_rcp_f32_e32 v18, v24
	v_rcp_f32_e32 v22, v27
	v_rcp_f32_e32 v19, v19
	v_rcp_f32_e32 v23, v26
	v_exp_f32_e32 v146, v21
	v_exp_f32_e32 v147, v25
	s_mov_b32 s8, 0xc038aa3b
	s_mov_b32 s4, 0x4038aa3b
	v_mov_b64_e32 v[160:161], s[8:9]
	v_exp_f32_e32 v148, v29
	v_exp_f32_e32 v149, v33
	v_pk_fma_f32 v[20:21], v[138:139], s[4:5], v[160:161] op_sel_hi:[1,0,0]
	s_nop 0
	v_pk_mul_f32 v[214:215], v[20:21], v[18:19]
	v_pk_fma_f32 v[18:19], v[140:141], s[4:5], v[160:161] op_sel_hi:[1,0,0]
	s_nop 0
	v_pk_mul_f32 v[212:213], v[18:19], v[22:23]
	v_add_u32_e32 v231, s7, v229
	ds_read_b128 v[18:21], v231 offset:36928
	ds_read_b128 v[22:25], v231 offset:36944
	ds_read_b128 v[26:29], v231 offset:36960
	ds_read_b128 v[30:33], v231 offset:36976
	s_waitcnt lgkmcnt(5)
	v_mfma_f32_32x32x16_bf16 v[2:17], v[46:49], v[142:145], v[236:251]
	ds_read_b128 v[138:141], v159 offset:16384
	v_add_f32_e32 v162, 1.0, v146
	v_exp_f32_e32 v163, v215
	v_exp_f32_e32 v164, v214
	v_exp_f32_e32 v165, v213
	v_exp_f32_e32 v166, v212
	v_add_f32_e32 v142, 1.0, v147
	v_add_f32_e32 v143, 1.0, v148
	v_add_f32_e32 v144, 1.0, v149
	v_mfma_f32_32x32x16_bf16 v[2:17], v[42:45], v[130:133], v[2:17]
	ds_read_b128 v[146:149], v159 offset:16416
	v_fmac_f32_e32 v162, v162, v163
	v_fmac_f32_e32 v142, v142, v164
	v_fmac_f32_e32 v143, v143, v165
	v_fmac_f32_e32 v144, v144, v166
	v_mfma_f32_32x32x16_bf16 v[2:17], v[38:41], v[154:157], v[2:17]
	ds_read_b128 v[150:153], v159 offset:16448
	v_rcp_f32_e32 v130, v162
	v_rcp_f32_e32 v131, v142
	v_rcp_f32_e32 v132, v143
	v_rcp_f32_e32 v133, v144
	s_waitcnt vmcnt(16)
	v_mfma_f32_32x32x16_bf16 v[2:17], v[34:37], v[134:137], v[2:17]
	ds_read_b128 v[178:181], v159 offset:16480
	v_fma_f32 v130, -v163, v130, v130
	v_fma_f32 v131, -v164, v131, v131
	v_fma_f32 v132, -v165, v132, v132
	v_fma_f32 v133, -v166, v133, v133
	v_add_u32_e32 v211, s6, v210
	v_cvt_pk_bf16_f32 v252, v130, v131
	v_cvt_pk_bf16_f32 v253, v132, v133
	s_nop 3
	v_exp_f32_e32 v131, v4
	v_exp_f32_e32 v130, v8
	v_exp_f32_e32 v133, v12
	v_exp_f32_e32 v132, v16
	v_exp_f32_e32 v2, v2
	v_exp_f32_e32 v4, v6
	v_exp_f32_e32 v6, v10
	v_exp_f32_e32 v7, v14
	v_add_f32_e32 v3, 1.0, v131
	v_add_f32_e32 v8, 1.0, v130
	v_add_f32_e32 v10, 1.0, v133
	v_add_f32_e32 v11, 1.0, v132
	v_fmac_f32_e32 v3, v2, v3
	v_fmac_f32_e32 v8, v4, v8
	v_fmac_f32_e32 v10, v6, v10
	v_fmac_f32_e32 v11, v7, v11
	v_rcp_f32_e32 v3, v3
	v_rcp_f32_e32 v2, v8
	v_rcp_f32_e32 v7, v10
	v_rcp_f32_e32 v6, v11
	v_exp_f32_e32 v134, v5
	v_exp_f32_e32 v135, v9
	v_pk_fma_f32 v[4:5], v[130:131], s[4:5], v[160:161] op_sel_hi:[1,0,0]
	v_exp_f32_e32 v130, v13
	v_pk_mul_f32 v[204:205], v[4:5], v[2:3]
	v_pk_fma_f32 v[2:3], v[132:133], s[4:5], v[160:161] op_sel_hi:[1,0,0]
	v_exp_f32_e32 v131, v17
	v_pk_mul_f32 v[202:203], v[2:3], v[6:7]
	s_waitcnt lgkmcnt(3)
	v_mfma_f32_32x32x16_bf16 v[18:33], v[94:97], v[138:141], v[18:33]
	v_add_f32_e32 v132, 1.0, v134
	v_exp_f32_e32 v133, v205
	v_add_f32_e32 v134, 1.0, v135
	v_exp_f32_e32 v135, v204
	v_exp_f32_e32 v136, v203
	v_exp_f32_e32 v137, v202
	v_add_f32_e32 v130, 1.0, v130
	v_add_f32_e32 v131, 1.0, v131
	s_waitcnt lgkmcnt(2)
	v_mfma_f32_32x32x16_bf16 v[18:33], v[90:93], v[146:149], v[18:33]
	v_fmac_f32_e32 v132, v132, v133
	v_fmac_f32_e32 v134, v134, v135
	v_fmac_f32_e32 v130, v130, v136
	v_fmac_f32_e32 v131, v131, v137
	s_waitcnt lgkmcnt(1)
	v_mfma_f32_32x32x16_bf16 v[18:33], v[86:89], v[150:153], v[18:33]
	v_rcp_f32_e32 v132, v132
	v_rcp_f32_e32 v134, v134
	v_rcp_f32_e32 v130, v130
	v_rcp_f32_e32 v131, v131
	s_waitcnt lgkmcnt(0)
	v_mfma_f32_32x32x16_bf16 v[18:33], v[82:85], v[178:181], v[18:33]
	v_fma_f32 v132, -v133, v132, v132
	v_fma_f32 v133, -v135, v134, v134
	v_fma_f32 v134, -v136, v130, v130
	v_fma_f32 v131, -v137, v131, v131
	v_cvt_pk_bf16_f32 v254, v132, v133
	v_cvt_pk_bf16_f32 v255, v134, v131
	ds_write_b128 v211, v[252:255] offset:0
	s_waitcnt lgkmcnt(0)
	s_barrier
	s_load_dwordx8 s[4:11], s[0:1], 0x10
	ds_read_b32 v229, v228 offset:31168
	ds_read_b128 v[174:177], v210
	v_add_u32_e32 v183, v230, v158
	ds_read_b128 v[170:173], v210 offset:1024
	v_exp_f32_e32 v131, v20
	v_exp_f32_e32 v130, v24
	v_exp_f32_e32 v133, v28
	v_exp_f32_e32 v132, v32
	ds_read_b128 v[166:169], v210 offset:2048
	v_exp_f32_e32 v18, v18
	v_exp_f32_e32 v20, v22
	v_exp_f32_e32 v22, v26
	v_exp_f32_e32 v23, v30
	v_fma_f32 v19, v131, s12, s12
	v_fma_f32 v24, v130, s12, s12
	v_fma_f32 v26, v133, s12, s12
	v_fma_f32 v27, v132, s12, s12
	ds_read_b128 v[162:165], v210 offset:3072
	v_fmac_f32_e32 v19, v18, v19
	v_fmac_f32_e32 v24, v20, v24
	v_fmac_f32_e32 v26, v22, v26
	v_fmac_f32_e32 v27, v23, v27
	ds_read_b128 v[158:161], v210 offset:4096
	v_rcp_f32_e32 v19, v19
	v_rcp_f32_e32 v18, v24
	v_rcp_f32_e32 v23, v26
	v_rcp_f32_e32 v22, v27
	ds_read_b128 v[154:157], v210 offset:5120
	v_exp_f32_e32 v186, v21
	v_exp_f32_e32 v187, v25
	ds_read_b128 v[142:145], v210 offset:6144
	s_mov_b32 s0, 0xc038aa3b
	v_exp_f32_e32 v188, v29
	v_pk_fma_f32 v[200:201], v[130:131], v[18:19], v[18:19] neg_lo:[1,0,0] neg_hi:[1,0,0]
	v_exp_f32_e32 v189, v33
	v_pk_fma_f32 v[198:199], v[132:133], v[22:23], v[22:23] neg_lo:[1,0,0] neg_hi:[1,0,0]
	ds_read_b128 v[130:133], v210 offset:7168
	ds_read_b128 v[18:21], v231 offset:36928
	ds_read_b128 v[22:25], v231 offset:36944
	ds_read_b128 v[26:29], v231 offset:36960
	ds_read_b128 v[30:33], v231 offset:36976
	v_mfma_f32_32x32x16_bf16 v[2:17], v[46:49], v[138:141], v[236:251]
	ds_read_b128 v[134:137], v183 offset:16384
	v_add_f32_e32 v186, 1.0, v186
	v_exp_f32_e32 v190, v201
	v_exp_f32_e32 v191, v200
	v_exp_f32_e32 v192, v199
	v_exp_f32_e32 v193, v198
	v_add_f32_e32 v187, 1.0, v187
	v_add_f32_e32 v188, 1.0, v188
	v_add_f32_e32 v189, 1.0, v189
	v_mfma_f32_32x32x16_bf16 v[2:17], v[42:45], v[146:149], v[2:17]
	ds_read_b128 v[138:141], v183 offset:16416
	v_fmac_f32_e32 v186, v186, v190
	v_fmac_f32_e32 v187, v187, v191
	v_fmac_f32_e32 v188, v188, v192
	v_fmac_f32_e32 v189, v189, v193
	v_mfma_f32_32x32x16_bf16 v[2:17], v[38:41], v[150:153], v[2:17]
	ds_read_b128 v[146:149], v183 offset:16448
	v_rcp_f32_e32 v186, v186
	v_rcp_f32_e32 v187, v187
	v_rcp_f32_e32 v188, v188
	v_rcp_f32_e32 v189, v189
	v_mfma_f32_32x32x16_bf16 v[2:17], v[34:37], v[178:181], v[2:17]
	ds_read_b128 v[150:153], v183 offset:16480
	v_fma_f32 v183, -v190, v186, v186
	v_fma_f32 v186, -v191, v187, v187
	v_fma_f32 v187, -v192, v188, v188
	v_fma_f32 v188, -v193, v189, v189
	s_waitcnt vmcnt(15) lgkmcnt(0)
	v_mfma_f32_32x32x16_bf16 v[18:33], v[126:129], v[174:177], v[18:33]
	v_cvt_pk_bf16_f32 v252, v183, v186
	v_cvt_pk_bf16_f32 v253, v187, v188
	s_waitcnt vmcnt(14)
	v_mfma_f32_32x32x16_bf16 v[18:33], v[122:125], v[170:173], v[18:33]
	s_nop 0
	v_exp_f32_e32 v179, v4
	v_exp_f32_e32 v178, v8
	v_exp_f32_e32 v181, v12
	v_exp_f32_e32 v180, v16
	s_waitcnt vmcnt(13)
	v_mfma_f32_32x32x16_bf16 v[18:33], v[118:121], v[166:169], v[18:33]
	v_exp_f32_e32 v2, v2
	v_exp_f32_e32 v4, v6
	v_exp_f32_e32 v7, v10
	v_exp_f32_e32 v8, v14
	v_fma_f32 v3, v179, s12, s12
	v_fma_f32 v6, v178, s12, s12
	v_fma_f32 v10, v181, s12, s12
	v_fma_f32 v11, v180, s12, s12
	s_waitcnt vmcnt(12)
	v_mfma_f32_32x32x16_bf16 v[18:33], v[114:117], v[162:165], v[18:33]
	v_fmac_f32_e32 v3, v2, v3
	v_fmac_f32_e32 v6, v4, v6
	v_fmac_f32_e32 v10, v7, v10
	v_fmac_f32_e32 v11, v8, v11
	s_waitcnt vmcnt(11)
	v_mfma_f32_32x32x16_bf16 v[18:33], v[110:113], v[158:161], v[18:33]
	v_rcp_f32_e32 v3, v3
	v_rcp_f32_e32 v2, v6
	v_rcp_f32_e32 v7, v10
	v_rcp_f32_e32 v6, v11
	s_waitcnt vmcnt(10)
	v_mfma_f32_32x32x16_bf16 v[18:33], v[106:109], v[154:157], v[18:33]
	v_exp_f32_e32 v183, v5
	v_exp_f32_e32 v186, v9
	s_waitcnt vmcnt(9)
	v_mfma_f32_32x32x16_bf16 v[18:33], v[102:105], v[142:145], v[18:33]
	v_pk_fma_f32 v[206:207], v[178:179], v[2:3], v[2:3] neg_lo:[1,0,0] neg_hi:[1,0,0]
	v_exp_f32_e32 v178, v13
	v_exp_f32_e32 v179, v17
	v_pk_fma_f32 v[208:209], v[180:181], v[6:7], v[6:7] neg_lo:[1,0,0] neg_hi:[1,0,0]
	s_waitcnt vmcnt(8)
	v_mfma_f32_32x32x16_bf16 v[18:33], v[98:101], v[130:133], v[18:33]
	v_mfma_f32_32x32x16_bf16 v[18:33], v[94:97], v[134:137], v[18:33]
	v_add_f32_e32 v180, 1.0, v183
	v_exp_f32_e32 v181, v207
	v_add_f32_e32 v183, 1.0, v186
	v_exp_f32_e32 v184, v206
	v_exp_f32_e32 v185, v209
	v_exp_f32_e32 v186, v208
	v_add_f32_e32 v178, 1.0, v178
	v_add_f32_e32 v179, 1.0, v179
	v_mfma_f32_32x32x16_bf16 v[18:33], v[90:93], v[138:141], v[18:33]
	v_fmac_f32_e32 v180, v180, v181
	v_fmac_f32_e32 v183, v183, v184
	v_fmac_f32_e32 v178, v178, v185
	v_fmac_f32_e32 v179, v179, v186
	v_mfma_f32_32x32x16_bf16 v[18:33], v[86:89], v[146:149], v[18:33]
	v_rcp_f32_e32 v180, v180
	v_rcp_f32_e32 v183, v183
	v_rcp_f32_e32 v178, v178
	v_rcp_f32_e32 v179, v179
	v_mfma_f32_32x32x16_bf16 v[18:33], v[82:85], v[150:153], v[18:33]
	v_fma_f32 v180, -v181, v180, v180
	v_fma_f32 v181, -v184, v183, v183
	v_fma_f32 v183, -v185, v178, v178
	v_fma_f32 v179, -v186, v179, v179
	v_cvt_pk_bf16_f32 v254, v180, v181
	v_cvt_pk_bf16_f32 v255, v183, v179
	ds_write_b128 v211, v[252:255] offset:8192
	s_waitcnt lgkmcnt(0)
	s_barrier
	v_mov_b32_e32 v178, 0x7a40
	v_lshl_add_u32 v232, v182, 2, v178
	s_mov_b32 s1, -1
	s_branch .LBB1_14
.LBB1_13:
	v_mfma_f32_32x32x16_bf16 v[2:17], v[78:81], v[206:209], v[236:251]
	ds_read_b128 v[174:177], v210
	v_add_u32_e32 v195, v230, v228
	v_mfma_f32_32x32x16_bf16 v[2:17], v[74:77], v[190:193], v[2:17]
	ds_read_b128 v[170:173], v210 offset:1024
	v_exp_f32_e32 v199, v28
	v_exp_f32_e32 v198, v32
	v_exp_f32_e32 v197, v20
	v_exp_f32_e32 v196, v24
	v_mfma_f32_32x32x16_bf16 v[2:17], v[70:73], v[158:161], v[2:17]
	ds_read_b128 v[166:169], v210 offset:2048
	v_exp_f32_e32 v18, v18
	v_exp_f32_e32 v22, v22
	v_exp_f32_e32 v24, v26
	v_exp_f32_e32 v26, v30
	v_fma_f32 v20, v197, s12, s12
	v_fma_f32 v28, v196, s12, s12
	v_fma_f32 v30, v199, s12, s12
	v_fma_f32 v32, v198, s12, s12
	v_mfma_f32_32x32x16_bf16 v[2:17], v[66:69], v[142:145], v[2:17]
	ds_read_b128 v[162:165], v210 offset:3072
	v_exp_f32_e32 v19, v19
	v_exp_f32_e32 v23, v23
	v_exp_f32_e32 v27, v27
	v_exp_f32_e32 v31, v31
	v_fmac_f32_e32 v20, v18, v20
	v_fmac_f32_e32 v28, v22, v28
	v_fmac_f32_e32 v30, v24, v30
	v_fmac_f32_e32 v32, v26, v32
	v_mfma_f32_32x32x16_bf16 v[2:17], v[62:65], v[154:157], v[2:17]
	ds_read_b128 v[158:161], v210 offset:4096
	v_add_f32_e32 v22, 1.0, v19
	v_rcp_f32_e32 v19, v20
	v_rcp_f32_e32 v18, v28
	v_add_f32_e32 v20, 1.0, v23
	v_rcp_f32_e32 v191, v30
	v_rcp_f32_e32 v190, v32
	v_mfma_f32_32x32x16_bf16 v[2:17], v[58:61], v[182:185], v[2:17]
	ds_read_b128 v[154:157], v210 offset:5120
	v_exp_f32_e32 v206, v21
	v_exp_f32_e32 v207, v25
	v_add_f32_e32 v23, 1.0, v27
	v_rcp_f32_e32 v192, v20
	v_add_f32_e32 v20, 1.0, v31
	v_rcp_f32_e32 v193, v22
	v_mfma_f32_32x32x16_bf16 v[2:17], v[54:57], v[186:189], v[2:17]
	ds_read_b128 v[142:145], v210 offset:6144
	v_exp_f32_e32 v208, v29
	v_exp_f32_e32 v209, v33
	v_rcp_f32_e32 v183, v23
	v_rcp_f32_e32 v182, v20
	v_mfma_f32_32x32x16_bf16 v[2:17], v[50:53], v[134:137], v[2:17]
	ds_read_b128 v[130:133], v210 offset:7168
	v_fma_f32 v186, -v196, v18, v18
	v_fma_f32 v187, -v197, v19, v19
	ds_read_b128 v[18:21], v231 offset:36928
	ds_read_b128 v[22:25], v231 offset:36944
	ds_read_b128 v[26:29], v231 offset:36960
	ds_read_b128 v[30:33], v231 offset:36976
	v_pk_fma_f32 v[200:201], v[192:193], v[220:221], v[186:187]
	v_pk_fma_f32 v[134:135], v[198:199], v[190:191], v[190:191] neg_lo:[1,0,0] neg_hi:[1,0,0]
	s_nop 0
	v_pk_fma_f32 v[198:199], v[182:183], v[222:223], v[134:135]
	v_mfma_f32_32x32x16_bf16 v[2:17], v[46:49], v[138:141], v[2:17]
	ds_read_b128 v[134:137], v195 offset:16384
	v_add_f32_e32 v182, 1.0, v206
	v_exp_f32_e32 v183, v201
	v_exp_f32_e32 v186, v200
	v_exp_f32_e32 v187, v199
	v_exp_f32_e32 v188, v198
	v_add_f32_e32 v189, 1.0, v207
	v_add_f32_e32 v190, 1.0, v208
	v_add_f32_e32 v191, 1.0, v209
	v_mfma_f32_32x32x16_bf16 v[2:17], v[42:45], v[146:149], v[2:17]
	ds_read_b128 v[138:141], v195 offset:16416
	v_fmac_f32_e32 v182, v182, v183
	v_fmac_f32_e32 v189, v189, v186
	v_fmac_f32_e32 v190, v190, v187
	v_fmac_f32_e32 v191, v191, v188
	v_mfma_f32_32x32x16_bf16 v[2:17], v[38:41], v[150:153], v[2:17]
	ds_read_b128 v[146:149], v195 offset:16448
	v_rcp_f32_e32 v182, v182
	v_rcp_f32_e32 v189, v189
	v_rcp_f32_e32 v190, v190
	v_rcp_f32_e32 v191, v191
	v_mfma_f32_32x32x16_bf16 v[2:17], v[34:37], v[178:181], v[2:17]
	ds_read_b128 v[150:153], v195 offset:16480
	v_fma_f32 v182, -v183, v182, v182
	v_fma_f32 v183, -v186, v189, v189
	v_fma_f32 v186, -v187, v190, v190
	v_fma_f32 v187, -v188, v191, v191
	s_waitcnt lgkmcnt(4)
	v_mfma_f32_32x32x16_bf16 v[18:33], v[126:129], v[174:177], v[18:33]
	v_cvt_pk_bf16_f32 v252, v182, v183
	v_cvt_pk_bf16_f32 v253, v186, v187
	v_mfma_f32_32x32x16_bf16 v[18:33], v[122:125], v[170:173], v[18:33]
	s_nop 1
	v_exp_f32_e32 v179, v4
	v_exp_f32_e32 v178, v8
	v_exp_f32_e32 v181, v12
	v_exp_f32_e32 v180, v16
	v_mfma_f32_32x32x16_bf16 v[18:33], v[118:121], v[166:169], v[18:33]
	v_exp_f32_e32 v2, v2
	v_exp_f32_e32 v6, v6
	v_exp_f32_e32 v10, v10
	v_exp_f32_e32 v12, v14
	v_fma_f32 v4, v179, s12, s12
	v_fma_f32 v8, v178, s12, s12
	v_fma_f32 v14, v181, s12, s12
	v_fma_f32 v16, v180, s12, s12
	v_mfma_f32_32x32x16_bf16 v[18:33], v[114:117], v[162:165], v[18:33]
	v_exp_f32_e32 v3, v3
	v_fmac_f32_e32 v4, v2, v4
	v_exp_f32_e32 v2, v7
	v_fmac_f32_e32 v8, v6, v8
	v_exp_f32_e32 v6, v11
	v_exp_f32_e32 v7, v15
	v_fmac_f32_e32 v14, v10, v14
	v_fmac_f32_e32 v16, v12, v16
	v_mfma_f32_32x32x16_bf16 v[18:33], v[110:113], v[158:161], v[18:33]
	v_add_f32_e32 v10, 1.0, v3
	v_rcp_f32_e32 v3, v4
	v_add_f32_e32 v4, 1.0, v2
	v_rcp_f32_e32 v2, v8
	v_rcp_f32_e32 v183, v14
	v_rcp_f32_e32 v182, v16
	v_mfma_f32_32x32x16_bf16 v[18:33], v[106:109], v[154:157], v[18:33]
	v_add_f32_e32 v6, 1.0, v6
	v_add_f32_e32 v7, 1.0, v7
	v_rcp_f32_e32 v187, v10
	v_rcp_f32_e32 v186, v4
	v_exp_f32_e32 v190, v5
	v_exp_f32_e32 v191, v9
	v_mfma_f32_32x32x16_bf16 v[18:33], v[102:105], v[142:145], v[18:33]
	v_rcp_f32_e32 v189, v6
	v_rcp_f32_e32 v188, v7
	v_exp_f32_e32 v192, v13
	v_exp_f32_e32 v193, v17
	v_mfma_f32_32x32x16_bf16 v[18:33], v[98:101], v[130:133], v[18:33]
	v_fma_f32 v178, -v178, v2, v2
	v_fma_f32 v179, -v179, v3, v3
	v_pk_fma_f32 v[206:207], v[186:187], v[216:217], v[178:179]
	s_nop 0
	v_pk_fma_f32 v[178:179], v[180:181], v[182:183], v[182:183] neg_lo:[1,0,0] neg_hi:[1,0,0]
	s_nop 0
	v_pk_fma_f32 v[208:209], v[188:189], v[218:219], v[178:179]
	s_waitcnt lgkmcnt(3)
	v_mfma_f32_32x32x16_bf16 v[18:33], v[94:97], v[134:137], v[18:33]
	v_add_f32_e32 v178, 1.0, v190
	v_exp_f32_e32 v179, v207
	v_add_f32_e32 v180, 1.0, v191
	v_exp_f32_e32 v181, v206
	v_exp_f32_e32 v182, v209
	v_exp_f32_e32 v183, v208
	v_add_f32_e32 v184, 1.0, v192
	v_add_f32_e32 v185, 1.0, v193
	s_waitcnt lgkmcnt(2)
	v_mfma_f32_32x32x16_bf16 v[18:33], v[90:93], v[138:141], v[18:33]
	v_fmac_f32_e32 v178, v178, v179
	v_fmac_f32_e32 v180, v180, v181
	v_fmac_f32_e32 v184, v184, v182
	v_fmac_f32_e32 v185, v185, v183
	s_waitcnt lgkmcnt(1)
	v_mfma_f32_32x32x16_bf16 v[18:33], v[86:89], v[146:149], v[18:33]
	v_rcp_f32_e32 v178, v178
	v_rcp_f32_e32 v180, v180
	v_rcp_f32_e32 v184, v184
	v_rcp_f32_e32 v185, v185
	s_waitcnt lgkmcnt(0)
	v_mfma_f32_32x32x16_bf16 v[18:33], v[82:85], v[150:153], v[18:33]
	v_fma_f32 v178, -v179, v178, v178
	v_fma_f32 v179, -v181, v180, v180
	v_fma_f32 v180, -v182, v184, v184
	v_fma_f32 v181, -v183, v185, v185
	v_cvt_pk_bf16_f32 v254, v178, v179
	v_cvt_pk_bf16_f32 v255, v180, v181
	ds_write_b128 v211, v[252:255] offset:8192
	s_waitcnt lgkmcnt(0)
	s_barrier
	s_add_i32 s1, s1, 2
	s_cmp_gt_u32 s1, 16
	v_add_u32_e32 v232, 0x200, v232
	s_cbranch_scc1 .LBB1_30
.LBB1_14:
	s_waitcnt vmcnt(7)
	v_mfma_f32_32x32x16_bf16 v[2:17], v[78:81], v[174:177], v[236:251]
	v_add_u32_e32 v192, v230, v229
	ds_read2_b32 v[228:229], v232 offset1:32
	ds_read_b128 v[194:197], v210 offset:8192
	s_waitcnt vmcnt(6)
	v_mfma_f32_32x32x16_bf16 v[2:17], v[74:77], v[170:173], v[2:17]
	ds_read_b128 v[178:181], v210 offset:9216
	v_exp_f32_e32 v187, v20
	v_exp_f32_e32 v186, v24
	v_exp_f32_e32 v189, v28
	v_exp_f32_e32 v188, v32
	s_waitcnt vmcnt(5)
	v_mfma_f32_32x32x16_bf16 v[2:17], v[70:73], v[166:169], v[2:17]
	ds_read_b128 v[170:173], v210 offset:10240
	v_exp_f32_e32 v18, v18
	v_exp_f32_e32 v22, v22
	v_exp_f32_e32 v24, v26
	v_exp_f32_e32 v26, v30
	v_fma_f32 v20, v187, s12, s12
	v_fma_f32 v28, v186, s12, s12
	v_fma_f32 v30, v189, s12, s12
	v_fma_f32 v32, v188, s12, s12
	s_waitcnt vmcnt(4)
	v_mfma_f32_32x32x16_bf16 v[2:17], v[66:69], v[162:165], v[2:17]
	ds_read_b128 v[166:169], v210 offset:11264
	v_exp_f32_e32 v19, v19
	v_exp_f32_e32 v23, v23
	v_exp_f32_e32 v27, v27
	v_exp_f32_e32 v31, v31
	v_fmac_f32_e32 v20, v18, v20
	v_fmac_f32_e32 v28, v22, v28
	v_fmac_f32_e32 v30, v24, v30
	v_fmac_f32_e32 v32, v26, v32
	s_waitcnt vmcnt(3)
	v_mfma_f32_32x32x16_bf16 v[2:17], v[62:65], v[158:161], v[2:17]
	ds_read_b128 v[162:165], v210 offset:12288
	v_add_f32_e32 v22, 1.0, v19
	v_rcp_f32_e32 v19, v20
	v_rcp_f32_e32 v18, v28
	v_rcp_f32_e32 v191, v30
	v_rcp_f32_e32 v190, v32
	v_add_f32_e32 v20, 1.0, v23
	s_waitcnt vmcnt(2)
	v_mfma_f32_32x32x16_bf16 v[2:17], v[58:61], v[154:157], v[2:17]
	ds_read_b128 v[174:177], v210 offset:13312
	v_rcp_f32_e32 v159, v22
	v_rcp_f32_e32 v158, v20
	v_exp_f32_e32 v160, v21
	v_exp_f32_e32 v161, v25
	v_add_f32_e32 v23, 1.0, v27
	v_add_f32_e32 v20, 1.0, v31
	s_waitcnt vmcnt(1)
	v_mfma_f32_32x32x16_bf16 v[2:17], v[54:57], v[142:145], v[2:17]
	ds_read_b128 v[182:185], v210 offset:14336
	v_rcp_f32_e32 v155, v23
	v_rcp_f32_e32 v154, v20
	v_exp_f32_e32 v193, v29
	v_exp_f32_e32 v217, v33
	s_waitcnt vmcnt(0)
	v_mfma_f32_32x32x16_bf16 v[2:17], v[50:53], v[130:133], v[2:17]
	ds_read_b128 v[142:145], v210 offset:15360
	v_fma_f32 v156, -v186, v18, v18
	v_fma_f32 v157, -v187, v19, v19
	ds_read_b128 v[18:21], v231 offset:36928
	ds_read_b128 v[22:25], v231 offset:36944
	ds_read_b128 v[26:29], v231 offset:36960
	ds_read_b128 v[30:33], v231 offset:36976
	v_pk_fma_f32 v[214:215], v[158:159], v[214:215], v[156:157]
	v_pk_fma_f32 v[130:131], v[188:189], v[190:191], v[190:191] neg_lo:[1,0,0] neg_hi:[1,0,0]
	s_nop 0
	v_pk_fma_f32 v[212:213], v[154:155], v[212:213], v[130:131]
	v_mfma_f32_32x32x16_bf16 v[2:17], v[46:49], v[134:137], v[2:17]
	ds_read_b128 v[154:157], v192 offset:16384
	v_add_f32_e32 v130, 1.0, v160
	v_exp_f32_e32 v131, v215
	v_exp_f32_e32 v132, v214
	v_exp_f32_e32 v133, v213
	v_exp_f32_e32 v220, v212
	v_add_f32_e32 v134, 1.0, v161
	v_add_f32_e32 v135, 1.0, v193
	v_add_f32_e32 v136, 1.0, v217
	v_mfma_f32_32x32x16_bf16 v[2:17], v[42:45], v[138:141], v[2:17]
	ds_read_b128 v[158:161], v192 offset:16416
	v_fmac_f32_e32 v130, v130, v131
	v_fmac_f32_e32 v134, v134, v132
	v_fmac_f32_e32 v135, v135, v133
	v_fmac_f32_e32 v136, v136, v220
	v_mfma_f32_32x32x16_bf16 v[2:17], v[38:41], v[146:149], v[2:17]
	ds_read_b128 v[186:189], v192 offset:16448
	v_rcp_f32_e32 v130, v130
	v_rcp_f32_e32 v134, v134
	v_rcp_f32_e32 v135, v135
	v_rcp_f32_e32 v136, v136
	v_mfma_f32_32x32x16_bf16 v[2:17], v[34:37], v[150:153], v[2:17]
	ds_read_b128 v[190:193], v192 offset:16480
	v_fma_f32 v130, -v131, v130, v130
	v_fma_f32 v131, -v132, v134, v134
	v_fma_f32 v132, -v133, v135, v135
	v_fma_f32 v133, -v220, v136, v136
	s_waitcnt lgkmcnt(4)
	v_mfma_f32_32x32x16_bf16 v[18:33], v[126:129], v[194:197], v[18:33]
	v_cvt_pk_bf16_f32 v252, v130, v131
	v_cvt_pk_bf16_f32 v253, v132, v133
	v_mfma_f32_32x32x16_bf16 v[18:33], v[122:125], v[178:181], v[18:33]
	s_nop 1
	v_exp_f32_e32 v131, v4
	v_exp_f32_e32 v130, v8
	v_exp_f32_e32 v133, v12
	v_exp_f32_e32 v132, v16
	v_mfma_f32_32x32x16_bf16 v[18:33], v[118:121], v[170:173], v[18:33]
	v_exp_f32_e32 v2, v2
	v_exp_f32_e32 v6, v6
	v_exp_f32_e32 v10, v10
	v_exp_f32_e32 v12, v14
	v_fma_f32 v4, v131, s12, s12
	v_fma_f32 v8, v130, s12, s12
	v_fma_f32 v14, v133, s12, s12
	v_fma_f32 v16, v132, s12, s12
	v_mfma_f32_32x32x16_bf16 v[18:33], v[114:117], v[166:169], v[18:33]
	v_exp_f32_e32 v3, v3
	v_fmac_f32_e32 v4, v2, v4
	v_exp_f32_e32 v2, v7
	v_fmac_f32_e32 v8, v6, v8
	v_exp_f32_e32 v6, v11
	v_exp_f32_e32 v7, v15
	v_fmac_f32_e32 v14, v10, v14
	v_fmac_f32_e32 v16, v12, v16
	v_mfma_f32_32x32x16_bf16 v[18:33], v[110:113], v[162:165], v[18:33]
	v_add_f32_e32 v10, 1.0, v3
	v_rcp_f32_e32 v3, v4
	v_add_f32_e32 v4, 1.0, v2
	v_rcp_f32_e32 v2, v8
	v_rcp_f32_e32 v135, v14
	v_rcp_f32_e32 v134, v16
	v_mfma_f32_32x32x16_bf16 v[18:33], v[106:109], v[174:177], v[18:33]
	v_add_f32_e32 v6, 1.0, v6
	v_add_f32_e32 v7, 1.0, v7
	v_rcp_f32_e32 v137, v10
	v_rcp_f32_e32 v136, v4
	v_exp_f32_e32 v140, v5
	v_exp_f32_e32 v141, v9
	v_mfma_f32_32x32x16_bf16 v[18:33], v[102:105], v[182:185], v[18:33]
	v_rcp_f32_e32 v139, v6
	v_rcp_f32_e32 v138, v7
	v_exp_f32_e32 v146, v13
	v_exp_f32_e32 v147, v17
	v_mfma_f32_32x32x16_bf16 v[18:33], v[98:101], v[142:145], v[18:33]
	v_fma_f32 v130, -v130, v2, v2
	v_fma_f32 v131, -v131, v3, v3
	v_pk_fma_f32 v[224:225], v[136:137], v[204:205], v[130:131]
	s_nop 0
	v_pk_fma_f32 v[130:131], v[132:133], v[134:135], v[134:135] neg_lo:[1,0,0] neg_hi:[1,0,0]
	s_nop 0
	v_pk_fma_f32 v[226:227], v[138:139], v[202:203], v[130:131]
	s_waitcnt lgkmcnt(3)
	v_mfma_f32_32x32x16_bf16 v[18:33], v[94:97], v[154:157], v[18:33]
	v_add_f32_e32 v130, 1.0, v140
	v_exp_f32_e32 v131, v225
	v_add_f32_e32 v132, 1.0, v141
	v_exp_f32_e32 v133, v224
	v_exp_f32_e32 v134, v227
	v_exp_f32_e32 v135, v226
	v_add_f32_e32 v136, 1.0, v146
	v_add_f32_e32 v137, 1.0, v147
	s_waitcnt lgkmcnt(2)
	v_mfma_f32_32x32x16_bf16 v[18:33], v[90:93], v[158:161], v[18:33]
	v_fmac_f32_e32 v130, v130, v131
	v_fmac_f32_e32 v132, v132, v133
	v_fmac_f32_e32 v136, v136, v134
	v_fmac_f32_e32 v137, v137, v135
	s_waitcnt lgkmcnt(1)
	v_mfma_f32_32x32x16_bf16 v[18:33], v[86:89], v[186:189], v[18:33]
	v_rcp_f32_e32 v130, v130
	v_rcp_f32_e32 v132, v132
	v_rcp_f32_e32 v136, v136
	v_rcp_f32_e32 v137, v137
	s_waitcnt lgkmcnt(0)
	v_mfma_f32_32x32x16_bf16 v[18:33], v[82:85], v[190:193], v[18:33]
	v_fma_f32 v130, -v131, v130, v130
	v_fma_f32 v131, -v133, v132, v132
	v_fma_f32 v132, -v134, v136, v136
	v_fma_f32 v133, -v135, v137, v137
	v_cvt_pk_bf16_f32 v254, v130, v131
	v_cvt_pk_bf16_f32 v255, v132, v133
	ds_write_b128 v211, v[252:255] offset:0
	s_waitcnt lgkmcnt(0)
	s_barrier
	v_mfma_f32_32x32x16_bf16 v[2:17], v[78:81], v[194:197], v[236:251]
	ds_read_b128 v[202:205], v210
	v_add_u32_e32 v216, v230, v228
	v_mfma_f32_32x32x16_bf16 v[2:17], v[74:77], v[178:181], v[2:17]
	ds_read_b128 v[194:197], v210 offset:1024
	v_exp_f32_e32 v147, v20
	v_exp_f32_e32 v146, v24
	v_exp_f32_e32 v149, v28
	v_exp_f32_e32 v148, v32
	v_mfma_f32_32x32x16_bf16 v[2:17], v[70:73], v[170:173], v[2:17]
	ds_read_b128 v[138:141], v210 offset:2048
	v_exp_f32_e32 v18, v18
	v_exp_f32_e32 v22, v22
	v_exp_f32_e32 v24, v26
	v_exp_f32_e32 v26, v30
	v_fma_f32 v20, v147, s12, s12
	v_fma_f32 v28, v146, s12, s12
	v_fma_f32 v30, v149, s12, s12
	v_fma_f32 v32, v148, s12, s12
	v_mfma_f32_32x32x16_bf16 v[2:17], v[66:69], v[166:169], v[2:17]
	ds_read_b128 v[134:137], v210 offset:3072
	v_exp_f32_e32 v19, v19
	v_exp_f32_e32 v23, v23
	v_exp_f32_e32 v27, v27
	v_exp_f32_e32 v31, v31
	v_fmac_f32_e32 v20, v18, v20
	v_fmac_f32_e32 v28, v22, v28
	v_fmac_f32_e32 v30, v24, v30
	v_fmac_f32_e32 v32, v26, v32
	v_mfma_f32_32x32x16_bf16 v[2:17], v[62:65], v[162:165], v[2:17]
	ds_read_b128 v[166:169], v210 offset:4096
	v_add_f32_e32 v22, 1.0, v19
	v_rcp_f32_e32 v19, v20
	v_rcp_f32_e32 v18, v28
	v_rcp_f32_e32 v151, v30
	v_rcp_f32_e32 v150, v32
	v_add_f32_e32 v20, 1.0, v23
	v_mfma_f32_32x32x16_bf16 v[2:17], v[58:61], v[174:177], v[2:17]
	ds_read_b128 v[162:165], v210 offset:5120
	v_rcp_f32_e32 v153, v22
	v_rcp_f32_e32 v152, v20
	v_add_f32_e32 v23, 1.0, v27
	v_add_f32_e32 v20, 1.0, v31
	v_exp_f32_e32 v180, v21
	v_exp_f32_e32 v181, v25
	v_mfma_f32_32x32x16_bf16 v[2:17], v[54:57], v[182:185], v[2:17]
	ds_read_b128 v[170:173], v210 offset:6144
	v_rcp_f32_e32 v175, v23
	v_rcp_f32_e32 v174, v20
	v_exp_f32_e32 v176, v29
	v_exp_f32_e32 v177, v33
	v_mfma_f32_32x32x16_bf16 v[2:17], v[50:53], v[142:145], v[2:17]
	ds_read_b128 v[130:133], v210 offset:7168
	v_fma_f32 v146, -v146, v18, v18
	v_fma_f32 v147, -v147, v19, v19
	ds_read_b128 v[18:21], v231 offset:36928
	ds_read_b128 v[22:25], v231 offset:36944
	ds_read_b128 v[26:29], v231 offset:36960
	ds_read_b128 v[30:33], v231 offset:36976
	v_pk_fma_f32 v[220:221], v[152:153], v[200:201], v[146:147]
	v_pk_fma_f32 v[142:143], v[148:149], v[150:151], v[150:151] neg_lo:[1,0,0] neg_hi:[1,0,0]
	s_nop 0
	v_pk_fma_f32 v[222:223], v[174:175], v[198:199], v[142:143]
	v_mfma_f32_32x32x16_bf16 v[2:17], v[46:49], v[154:157], v[2:17]
	ds_read_b128 v[146:149], v216 offset:16384
	v_add_f32_e32 v142, 1.0, v180
	v_exp_f32_e32 v143, v221
	v_exp_f32_e32 v144, v220
	v_exp_f32_e32 v145, v223
	v_exp_f32_e32 v180, v222
	v_add_f32_e32 v154, 1.0, v181
	v_add_f32_e32 v155, 1.0, v176
	v_add_f32_e32 v156, 1.0, v177
	v_mfma_f32_32x32x16_bf16 v[2:17], v[42:45], v[158:161], v[2:17]
	ds_read_b128 v[150:153], v216 offset:16416
	v_fmac_f32_e32 v142, v142, v143
	v_fmac_f32_e32 v154, v154, v144
	v_fmac_f32_e32 v155, v155, v145
	v_fmac_f32_e32 v156, v156, v180
	v_mfma_f32_32x32x16_bf16 v[2:17], v[38:41], v[186:189], v[2:17]
	ds_read_b128 v[174:177], v216 offset:16448
	v_rcp_f32_e32 v142, v142
	v_rcp_f32_e32 v154, v154
	v_rcp_f32_e32 v155, v155
	v_rcp_f32_e32 v156, v156
	v_mfma_f32_32x32x16_bf16 v[2:17], v[34:37], v[190:193], v[2:17]
	ds_read_b128 v[198:201], v216 offset:16480
	v_fma_f32 v142, -v143, v142, v142
	v_fma_f32 v143, -v144, v154, v154
	v_fma_f32 v144, -v145, v155, v155
	v_fma_f32 v145, -v180, v156, v156
	s_waitcnt lgkmcnt(4)
	v_mfma_f32_32x32x16_bf16 v[18:33], v[126:129], v[202:205], v[18:33]
	v_cvt_pk_bf16_f32 v252, v142, v143
	v_cvt_pk_bf16_f32 v253, v144, v145
	v_mfma_f32_32x32x16_bf16 v[18:33], v[122:125], v[194:197], v[18:33]
	s_nop 1
	v_exp_f32_e32 v143, v4
	v_exp_f32_e32 v142, v8
	v_exp_f32_e32 v145, v12
	v_exp_f32_e32 v144, v16
	v_mfma_f32_32x32x16_bf16 v[18:33], v[118:121], v[138:141], v[18:33]
	v_exp_f32_e32 v2, v2
	v_exp_f32_e32 v6, v6
	v_exp_f32_e32 v10, v10
	v_exp_f32_e32 v12, v14
	v_fma_f32 v4, v143, s12, s12
	v_fma_f32 v8, v142, s12, s12
	v_fma_f32 v14, v145, s12, s12
	v_fma_f32 v16, v144, s12, s12
	v_mfma_f32_32x32x16_bf16 v[18:33], v[114:117], v[134:137], v[18:33]
	v_exp_f32_e32 v3, v3
	v_fmac_f32_e32 v4, v2, v4
	v_exp_f32_e32 v2, v7
	v_fmac_f32_e32 v8, v6, v8
	v_exp_f32_e32 v6, v11
	v_exp_f32_e32 v7, v15
	v_fmac_f32_e32 v14, v10, v14
	v_fmac_f32_e32 v16, v12, v16
	v_mfma_f32_32x32x16_bf16 v[18:33], v[110:113], v[166:169], v[18:33]
	v_add_f32_e32 v10, 1.0, v3
	v_rcp_f32_e32 v3, v4
	v_add_f32_e32 v4, 1.0, v2
	v_rcp_f32_e32 v2, v8
	v_rcp_f32_e32 v155, v14
	v_rcp_f32_e32 v154, v16
	v_mfma_f32_32x32x16_bf16 v[18:33], v[106:109], v[162:165], v[18:33]
	v_add_f32_e32 v6, 1.0, v6
	v_add_f32_e32 v7, 1.0, v7
	v_rcp_f32_e32 v157, v10
	v_rcp_f32_e32 v156, v4
	v_exp_f32_e32 v160, v5
	v_exp_f32_e32 v161, v9
	v_mfma_f32_32x32x16_bf16 v[18:33], v[102:105], v[170:173], v[18:33]
	v_rcp_f32_e32 v159, v6
	v_rcp_f32_e32 v158, v7
	v_exp_f32_e32 v180, v13
	v_exp_f32_e32 v181, v17
	v_mfma_f32_32x32x16_bf16 v[18:33], v[98:101], v[130:133], v[18:33]
	v_fma_f32 v142, -v142, v2, v2
	v_fma_f32 v143, -v143, v3, v3
	v_pk_fma_f32 v[216:217], v[156:157], v[206:207], v[142:143]
	s_nop 0
	v_pk_fma_f32 v[142:143], v[144:145], v[154:155], v[154:155] neg_lo:[1,0,0] neg_hi:[1,0,0]
	s_nop 0
	v_pk_fma_f32 v[218:219], v[158:159], v[208:209], v[142:143]
	s_waitcnt lgkmcnt(3)
	v_mfma_f32_32x32x16_bf16 v[18:33], v[94:97], v[146:149], v[18:33]
	v_add_f32_e32 v142, 1.0, v160
	v_exp_f32_e32 v143, v217
	v_add_f32_e32 v144, 1.0, v161
	v_exp_f32_e32 v145, v216
	v_exp_f32_e32 v154, v219
	v_exp_f32_e32 v155, v218
	v_add_f32_e32 v156, 1.0, v180
	v_add_f32_e32 v157, 1.0, v181
	s_waitcnt lgkmcnt(2)
	v_mfma_f32_32x32x16_bf16 v[18:33], v[90:93], v[150:153], v[18:33]
	v_fmac_f32_e32 v142, v142, v143
	v_fmac_f32_e32 v144, v144, v145
	v_fmac_f32_e32 v156, v156, v154
	v_fmac_f32_e32 v157, v157, v155
	s_waitcnt lgkmcnt(1)
	v_mfma_f32_32x32x16_bf16 v[18:33], v[86:89], v[174:177], v[18:33]
	v_rcp_f32_e32 v142, v142
	v_rcp_f32_e32 v144, v144
	v_rcp_f32_e32 v156, v156
	v_rcp_f32_e32 v157, v157
	s_waitcnt lgkmcnt(0)
	v_mfma_f32_32x32x16_bf16 v[18:33], v[82:85], v[198:201], v[18:33]
	v_fma_f32 v142, -v143, v142, v142
	v_fma_f32 v143, -v145, v144, v144
	v_fma_f32 v144, -v154, v156, v156
	v_fma_f32 v145, -v155, v157, v157
	v_cvt_pk_bf16_f32 v254, v142, v143
	v_cvt_pk_bf16_f32 v255, v144, v145
	ds_write_b128 v211, v[252:255] offset:8192
	s_waitcnt lgkmcnt(0)
	s_barrier
	v_mfma_f32_32x32x16_bf16 v[2:17], v[78:81], v[202:205], v[236:251]
	v_add_u32_e32 v234, v230, v229
	ds_read2_b32 v[228:229], v232 offset0:64 offset1:96
	ds_read_b128 v[206:209], v210 offset:8192
	v_mfma_f32_32x32x16_bf16 v[2:17], v[74:77], v[194:197], v[2:17]
	ds_read_b128 v[190:193], v210 offset:9216
	v_exp_f32_e32 v179, v20
	v_exp_f32_e32 v178, v24
	v_exp_f32_e32 v181, v28
	v_exp_f32_e32 v180, v32
	v_mfma_f32_32x32x16_bf16 v[2:17], v[70:73], v[138:141], v[2:17]
	ds_read_b128 v[158:161], v210 offset:10240
	v_exp_f32_e32 v18, v18
	v_exp_f32_e32 v22, v22
	v_exp_f32_e32 v24, v26
	v_exp_f32_e32 v26, v30
	v_fma_f32 v20, v179, s12, s12
	v_fma_f32 v28, v178, s12, s12
	v_fma_f32 v30, v181, s12, s12
	v_fma_f32 v32, v180, s12, s12
	v_mfma_f32_32x32x16_bf16 v[2:17], v[66:69], v[134:137], v[2:17]
	ds_read_b128 v[142:145], v210 offset:11264
	v_exp_f32_e32 v19, v19
	v_exp_f32_e32 v23, v23
	v_exp_f32_e32 v27, v27
	v_exp_f32_e32 v31, v31
	v_fmac_f32_e32 v20, v18, v20
	v_fmac_f32_e32 v28, v22, v28
	v_fmac_f32_e32 v30, v24, v30
	v_fmac_f32_e32 v32, v26, v32
	v_mfma_f32_32x32x16_bf16 v[2:17], v[62:65], v[166:169], v[2:17]
	ds_read_b128 v[154:157], v210 offset:12288
	v_add_f32_e32 v22, 1.0, v19
	v_rcp_f32_e32 v19, v20
	v_rcp_f32_e32 v18, v28
	v_rcp_f32_e32 v139, v30
	v_rcp_f32_e32 v138, v32
	v_add_f32_e32 v20, 1.0, v23
	v_mfma_f32_32x32x16_bf16 v[2:17], v[58:61], v[162:165], v[2:17]
	ds_read_b128 v[182:185], v210 offset:13312
	v_rcp_f32_e32 v141, v22
	v_rcp_f32_e32 v140, v20
	v_add_f32_e32 v23, 1.0, v27
	v_add_f32_e32 v20, 1.0, v31
	v_exp_f32_e32 v168, v21
	v_exp_f32_e32 v169, v25
	v_mfma_f32_32x32x16_bf16 v[2:17], v[54:57], v[170:173], v[2:17]
	ds_read_b128 v[186:189], v210 offset:14336
	v_rcp_f32_e32 v163, v23
	v_rcp_f32_e32 v162, v20
	v_exp_f32_e32 v194, v29
	v_exp_f32_e32 v195, v33
	v_mfma_f32_32x32x16_bf16 v[2:17], v[50:53], v[130:133], v[2:17]
	ds_read_b128 v[134:137], v210 offset:15360
	v_fma_f32 v166, -v178, v18, v18
	v_fma_f32 v167, -v179, v19, v19
	ds_read_b128 v[18:21], v231 offset:36928
	ds_read_b128 v[22:25], v231 offset:36944
	ds_read_b128 v[26:29], v231 offset:36960
	ds_read_b128 v[30:33], v231 offset:36976
	v_pk_fma_f32 v[214:215], v[140:141], v[214:215], v[166:167]
	v_pk_fma_f32 v[130:131], v[180:181], v[138:139], v[138:139] neg_lo:[1,0,0] neg_hi:[1,0,0]
	s_nop 0
	v_pk_fma_f32 v[212:213], v[162:163], v[212:213], v[130:131]
	v_mfma_f32_32x32x16_bf16 v[2:17], v[46:49], v[146:149], v[2:17]
	ds_read_b128 v[138:141], v234 offset:16384
	v_add_f32_e32 v130, 1.0, v168
	v_exp_f32_e32 v131, v215
	v_exp_f32_e32 v132, v214
	v_exp_f32_e32 v133, v213
	v_exp_f32_e32 v162, v212
	v_add_f32_e32 v163, 1.0, v169
	v_add_f32_e32 v166, 1.0, v194
	v_add_f32_e32 v167, 1.0, v195
	v_mfma_f32_32x32x16_bf16 v[2:17], v[42:45], v[150:153], v[2:17]
	ds_read_b128 v[146:149], v234 offset:16416
	v_fmac_f32_e32 v130, v130, v131
	v_fmac_f32_e32 v163, v163, v132
	v_fmac_f32_e32 v166, v166, v133
	v_fmac_f32_e32 v167, v167, v162
	v_mfma_f32_32x32x16_bf16 v[2:17], v[38:41], v[174:177], v[2:17]
	ds_read_b128 v[150:153], v234 offset:16448
	v_rcp_f32_e32 v130, v130
	v_rcp_f32_e32 v163, v163
	v_rcp_f32_e32 v166, v166
	v_rcp_f32_e32 v167, v167
	v_mfma_f32_32x32x16_bf16 v[2:17], v[34:37], v[198:201], v[2:17]
	ds_read_b128 v[178:181], v234 offset:16480
	v_fma_f32 v130, -v131, v130, v130
	v_fma_f32 v131, -v132, v163, v163
	v_fma_f32 v132, -v133, v166, v166
	v_fma_f32 v133, -v162, v167, v167
	s_waitcnt lgkmcnt(4)
	v_mfma_f32_32x32x16_bf16 v[18:33], v[126:129], v[206:209], v[18:33]
	v_cvt_pk_bf16_f32 v252, v130, v131
	v_cvt_pk_bf16_f32 v253, v132, v133
	v_mfma_f32_32x32x16_bf16 v[18:33], v[122:125], v[190:193], v[18:33]
	s_nop 1
	v_exp_f32_e32 v131, v4
	v_exp_f32_e32 v130, v8
	v_exp_f32_e32 v133, v12
	v_exp_f32_e32 v132, v16
	v_mfma_f32_32x32x16_bf16 v[18:33], v[118:121], v[158:161], v[18:33]
	v_exp_f32_e32 v2, v2
	v_exp_f32_e32 v6, v6
	v_exp_f32_e32 v10, v10
	v_exp_f32_e32 v12, v14
	v_fma_f32 v4, v131, s12, s12
	v_fma_f32 v8, v130, s12, s12
	v_fma_f32 v14, v133, s12, s12
	v_fma_f32 v16, v132, s12, s12
	v_mfma_f32_32x32x16_bf16 v[18:33], v[114:117], v[142:145], v[18:33]
	v_exp_f32_e32 v3, v3
	v_fmac_f32_e32 v4, v2, v4
	v_exp_f32_e32 v2, v7
	v_fmac_f32_e32 v8, v6, v8
	v_exp_f32_e32 v6, v11
	v_exp_f32_e32 v7, v15
	v_fmac_f32_e32 v14, v10, v14
	v_fmac_f32_e32 v16, v12, v16
	v_mfma_f32_32x32x16_bf16 v[18:33], v[110:113], v[154:157], v[18:33]
	v_add_f32_e32 v10, 1.0, v3
	v_rcp_f32_e32 v3, v4
	v_add_f32_e32 v4, 1.0, v2
	v_rcp_f32_e32 v2, v8
	v_rcp_f32_e32 v163, v14
	v_rcp_f32_e32 v162, v16
	v_mfma_f32_32x32x16_bf16 v[18:33], v[106:109], v[182:185], v[18:33]
	v_add_f32_e32 v6, 1.0, v6
	v_add_f32_e32 v7, 1.0, v7
	v_rcp_f32_e32 v167, v10
	v_rcp_f32_e32 v166, v4
	v_exp_f32_e32 v170, v5
	v_exp_f32_e32 v171, v9
	v_mfma_f32_32x32x16_bf16 v[18:33], v[102:105], v[186:189], v[18:33]
	v_rcp_f32_e32 v169, v6
	v_rcp_f32_e32 v168, v7
	v_exp_f32_e32 v172, v13
	v_exp_f32_e32 v173, v17
	v_mfma_f32_32x32x16_bf16 v[18:33], v[98:101], v[134:137], v[18:33]
	v_fma_f32 v130, -v130, v2, v2
	v_fma_f32 v131, -v131, v3, v3
	v_pk_fma_f32 v[204:205], v[166:167], v[224:225], v[130:131]
	s_nop 0
	v_pk_fma_f32 v[130:131], v[132:133], v[162:163], v[162:163] neg_lo:[1,0,0] neg_hi:[1,0,0]
	s_nop 0
	v_pk_fma_f32 v[202:203], v[168:169], v[226:227], v[130:131]
	s_waitcnt lgkmcnt(3)
	v_mfma_f32_32x32x16_bf16 v[18:33], v[94:97], v[138:141], v[18:33]
	v_add_f32_e32 v130, 1.0, v170
	v_exp_f32_e32 v131, v205
	v_add_f32_e32 v132, 1.0, v171
	v_exp_f32_e32 v133, v204
	v_exp_f32_e32 v162, v203
	v_exp_f32_e32 v163, v202
	v_add_f32_e32 v164, 1.0, v172
	v_add_f32_e32 v165, 1.0, v173
	s_waitcnt lgkmcnt(2)
	v_mfma_f32_32x32x16_bf16 v[18:33], v[90:93], v[146:149], v[18:33]
	v_fmac_f32_e32 v130, v130, v131
	v_fmac_f32_e32 v132, v132, v133
	v_fmac_f32_e32 v164, v164, v162
	v_fmac_f32_e32 v165, v165, v163
	s_waitcnt lgkmcnt(1)
	v_mfma_f32_32x32x16_bf16 v[18:33], v[86:89], v[150:153], v[18:33]
	v_rcp_f32_e32 v130, v130
	v_rcp_f32_e32 v132, v132
	v_rcp_f32_e32 v164, v164
	v_rcp_f32_e32 v165, v165
	s_waitcnt lgkmcnt(0)
	v_mfma_f32_32x32x16_bf16 v[18:33], v[82:85], v[178:181], v[18:33]
	v_fma_f32 v130, -v131, v130, v130
	v_fma_f32 v131, -v133, v132, v132
	v_fma_f32 v132, -v162, v164, v164
	v_fma_f32 v133, -v163, v165, v165
	v_cvt_pk_bf16_f32 v254, v130, v131
	v_cvt_pk_bf16_f32 v255, v132, v133
	ds_write_b128 v211, v[252:255] offset:0
	s_waitcnt lgkmcnt(0)
	s_barrier
	s_branch .LBB1_13
.LBB1_30:
	v_mfma_f32_32x32x16_bf16 v[2:17], v[78:81], v[174:177], v[236:251]
	ds_read_b128 v[178:181], v210 offset:8192
	v_add_u32_e32 v182, v230, v229
	v_mfma_f32_32x32x16_bf16 v[2:17], v[74:77], v[170:173], v[2:17]
	ds_read_b128 v[174:177], v210 offset:9216
	v_exp_f32_e32 v20, v20
	v_exp_f32_e32 v24, v24
	v_exp_f32_e32 v28, v28
	v_exp_f32_e32 v32, v32
	v_mfma_f32_32x32x16_bf16 v[2:17], v[70:73], v[166:169], v[2:17]
	ds_read_b128 v[170:173], v210 offset:10240
	v_exp_f32_e32 v18, v18
	v_exp_f32_e32 v22, v22
	v_exp_f32_e32 v26, v26
	v_exp_f32_e32 v30, v30
	v_add_f32_e32 v183, 1.0, v20
	v_add_f32_e32 v184, 1.0, v24
	v_add_f32_e32 v185, 1.0, v28
	v_add_f32_e32 v186, 1.0, v32
	v_mfma_f32_32x32x16_bf16 v[2:17], v[66:69], v[162:165], v[2:17]
	ds_read_b128 v[166:169], v210 offset:11264
	v_exp_f32_e32 v19, v19
	v_fmac_f32_e32 v183, v18, v183
	v_exp_f32_e32 v18, v23
	v_exp_f32_e32 v23, v27
	v_exp_f32_e32 v27, v31
	v_fmac_f32_e32 v184, v22, v184
	v_fmac_f32_e32 v185, v26, v185
	v_fmac_f32_e32 v186, v30, v186
	v_mfma_f32_32x32x16_bf16 v[2:17], v[62:65], v[158:161], v[2:17]
	ds_read_b128 v[162:165], v210 offset:12288
	v_rcp_f32_e32 v22, v183
	v_rcp_f32_e32 v26, v184
	v_rcp_f32_e32 v30, v185
	v_rcp_f32_e32 v31, v186
	v_mov_b32_e32 v183, 0xc038aa3b
	v_add_f32_e32 v19, 1.0, v19
	v_fmamk_f32 v20, v20, 0x4038aa3b, v183
	v_add_f32_e32 v18, 1.0, v18
	v_fmamk_f32 v24, v24, 0x4038aa3b, v183
	v_mfma_f32_32x32x16_bf16 v[2:17], v[58:61], v[154:157], v[2:17]
	ds_read_b128 v[158:161], v210 offset:13312
	v_rcp_f32_e32 v19, v19
	v_add_f32_e32 v23, 1.0, v23
	v_rcp_f32_e32 v184, v18
	v_exp_f32_e32 v185, v21
	v_exp_f32_e32 v186, v25
	v_fmamk_f32 v18, v28, 0x4038aa3b, v183
	v_add_f32_e32 v21, 1.0, v27
	v_fmamk_f32 v25, v32, 0x4038aa3b, v183
	v_mfma_f32_32x32x16_bf16 v[2:17], v[54:57], v[142:145], v[2:17]
	ds_read_b128 v[154:157], v210 offset:14336
	v_mul_f32_e32 v187, v20, v22
	v_rcp_f32_e32 v188, v23
	v_rcp_f32_e32 v189, v21
	v_exp_f32_e32 v190, v29
	v_exp_f32_e32 v191, v33
	v_mul_f32_e32 v192, v24, v26
	v_mul_f32_e32 v193, v18, v30
	v_mul_f32_e32 v194, v25, v31
	v_mfma_f32_32x32x16_bf16 v[2:17], v[50:53], v[130:133], v[2:17]
	ds_read_b128 v[142:145], v210 offset:15360
	v_fmac_f32_e32 v187, v19, v215
	ds_read_b128 v[18:21], v231 offset:36928
	ds_read_b128 v[22:25], v231 offset:36944
	ds_read_b128 v[26:29], v231 offset:36960
	ds_read_b128 v[30:33], v231 offset:36976
	v_fmac_f32_e32 v192, v184, v214
	v_fmac_f32_e32 v193, v188, v213
	v_fmac_f32_e32 v194, v189, v212
	v_mfma_f32_32x32x16_bf16 v[2:17], v[46:49], v[134:137], v[2:17]
	ds_read_b128 v[130:133], v182 offset:16384
	v_add_f32_e32 v184, 1.0, v185
	v_exp_f32_e32 v185, v187
	v_exp_f32_e32 v187, v192
	v_exp_f32_e32 v188, v193
	v_exp_f32_e32 v189, v194
	v_add_f32_e32 v186, 1.0, v186
	v_add_f32_e32 v190, 1.0, v190
	v_add_f32_e32 v191, 1.0, v191
	v_mfma_f32_32x32x16_bf16 v[2:17], v[42:45], v[138:141], v[2:17]
	ds_read_b128 v[134:137], v182 offset:16416
	v_fmac_f32_e32 v184, v184, v185
	v_fmac_f32_e32 v186, v186, v187
	v_fmac_f32_e32 v190, v190, v188
	v_fmac_f32_e32 v191, v191, v189
	v_mfma_f32_32x32x16_bf16 v[2:17], v[38:41], v[146:149], v[2:17]
	ds_read_b128 v[138:141], v182 offset:16448
	v_rcp_f32_e32 v184, v184
	v_rcp_f32_e32 v186, v186
	v_rcp_f32_e32 v190, v190
	v_rcp_f32_e32 v191, v191
	v_mfma_f32_32x32x16_bf16 v[2:17], v[34:37], v[150:153], v[2:17]
	ds_read_b128 v[146:149], v182 offset:16480
	v_fma_f32 v182, -v185, v184, v184
	v_fma_f32 v184, -v187, v186, v186
	v_fma_f32 v185, -v188, v190, v190
	v_fma_f32 v186, -v189, v191, v191
	s_waitcnt lgkmcnt(4)
	v_mfma_f32_32x32x16_bf16 v[18:33], v[126:129], v[178:181], v[18:33]
	v_cvt_pk_bf16_f32 v252, v182, v184
	v_cvt_pk_bf16_f32 v253, v185, v186
	v_mfma_f32_32x32x16_bf16 v[18:33], v[122:125], v[174:177], v[18:33]
	s_nop 1
	v_exp_f32_e32 v4, v4
	v_exp_f32_e32 v8, v8
	v_exp_f32_e32 v12, v12
	v_exp_f32_e32 v16, v16
	v_mfma_f32_32x32x16_bf16 v[18:33], v[118:121], v[170:173], v[18:33]
	v_exp_f32_e32 v2, v2
	v_exp_f32_e32 v6, v6
	v_exp_f32_e32 v10, v10
	v_exp_f32_e32 v14, v14
	v_add_f32_e32 v122, 1.0, v4
	v_add_f32_e32 v123, 1.0, v8
	v_add_f32_e32 v118, 1.0, v12
	v_add_f32_e32 v119, 1.0, v16
	v_mfma_f32_32x32x16_bf16 v[18:33], v[114:117], v[166:169], v[18:33]
	v_exp_f32_e32 v3, v3
	v_fmac_f32_e32 v122, v2, v122
	v_exp_f32_e32 v2, v7
	v_fmac_f32_e32 v123, v6, v123
	v_exp_f32_e32 v6, v11
	v_exp_f32_e32 v7, v15
	v_fmac_f32_e32 v118, v10, v118
	v_fmac_f32_e32 v119, v14, v119
	v_mfma_f32_32x32x16_bf16 v[18:33], v[110:113], v[162:165], v[18:33]
	v_rcp_f32_e32 v10, v122
	v_rcp_f32_e32 v11, v123
	v_rcp_f32_e32 v14, v118
	v_rcp_f32_e32 v15, v119
	v_add_f32_e32 v3, 1.0, v3
	v_fmamk_f32 v4, v4, 0x4038aa3b, v183
	v_add_f32_e32 v2, 1.0, v2
	v_fmamk_f32 v8, v8, 0x4038aa3b, v183
	v_mfma_f32_32x32x16_bf16 v[18:33], v[106:109], v[158:161], v[18:33]
	v_rcp_f32_e32 v3, v3
	v_rcp_f32_e32 v2, v2
	v_add_f32_e32 v6, 1.0, v6
	v_fmamk_f32 v12, v12, 0x4038aa3b, v183
	v_exp_f32_e32 v110, v5
	v_add_f32_e32 v5, 1.0, v7
	v_exp_f32_e32 v111, v9
	v_fmac_f32_e32 v183, 0x4038aa3b, v16
	v_mfma_f32_32x32x16_bf16 v[18:33], v[102:105], v[154:157], v[18:33]
	v_mul_f32_e32 v106, v4, v10
	v_mul_f32_e32 v107, v8, v11
	v_rcp_f32_e32 v108, v6
	v_rcp_f32_e32 v109, v5
	v_exp_f32_e32 v112, v13
	v_exp_f32_e32 v113, v17
	v_mul_f32_e32 v102, v12, v14
	v_mul_f32_e32 v103, v183, v15
	v_mfma_f32_32x32x16_bf16 v[18:33], v[98:101], v[142:145], v[18:33]
	v_fmac_f32_e32 v106, v3, v205
	v_fmac_f32_e32 v107, v2, v204
	v_fmac_f32_e32 v102, v108, v203
	v_fmac_f32_e32 v103, v109, v202
	s_waitcnt lgkmcnt(3)
	v_mfma_f32_32x32x16_bf16 v[18:33], v[94:97], v[130:133], v[18:33]
	v_add_f32_e32 v98, 1.0, v110
	v_exp_f32_e32 v99, v106
	v_add_f32_e32 v100, 1.0, v111
	v_exp_f32_e32 v101, v107
	v_exp_f32_e32 v102, v102
	v_exp_f32_e32 v103, v103
	v_add_f32_e32 v94, 1.0, v112
	v_add_f32_e32 v95, 1.0, v113
	s_waitcnt lgkmcnt(2)
	v_mfma_f32_32x32x16_bf16 v[18:33], v[90:93], v[134:137], v[18:33]
	v_fmac_f32_e32 v98, v98, v99
	v_fmac_f32_e32 v100, v100, v101
	v_fmac_f32_e32 v94, v94, v102
	v_fmac_f32_e32 v95, v95, v103
	s_waitcnt lgkmcnt(1)
	v_mfma_f32_32x32x16_bf16 v[18:33], v[86:89], v[138:141], v[18:33]
	v_rcp_f32_e32 v90, v98
	v_rcp_f32_e32 v91, v100
	v_rcp_f32_e32 v92, v94
	v_rcp_f32_e32 v93, v95
	s_waitcnt lgkmcnt(0)
	v_mfma_f32_32x32x16_bf16 v[18:33], v[82:85], v[146:149], v[18:33]
	v_fma_f32 v86, -v99, v90, v90
	v_fma_f32 v87, -v101, v91, v91
	v_fma_f32 v88, -v102, v92, v92
	v_fma_f32 v89, -v103, v93, v93
	v_cvt_pk_bf16_f32 v254, v86, v87
	v_cvt_pk_bf16_f32 v255, v88, v89
	ds_write_b128 v211, v[252:255] offset:0
	s_waitcnt lgkmcnt(0)
	s_barrier
	v_mfma_f32_32x32x16_bf16 v[2:17], v[78:81], v[178:181], v[236:251]
	v_exp_f32_e32 v20, v20
	v_exp_f32_e32 v24, v24
	v_exp_f32_e32 v28, v28
	v_exp_f32_e32 v32, v32
	v_mfma_f32_32x32x16_bf16 v[2:17], v[74:77], v[174:177], v[2:17]
	v_exp_f32_e32 v18, v18
	v_add_f32_e32 v74, 1.0, v20
	v_exp_f32_e32 v22, v22
	v_add_f32_e32 v75, 1.0, v24
	v_exp_f32_e32 v26, v26
	v_exp_f32_e32 v30, v30
	v_mfma_f32_32x32x16_bf16 v[2:17], v[70:73], v[170:173], v[2:17]
	v_add_f32_e32 v70, 1.0, v28
	v_add_f32_e32 v71, 1.0, v32
	v_exp_f32_e32 v19, v19
	v_fmac_f32_e32 v74, v18, v74
	v_exp_f32_e32 v18, v23
	v_fmac_f32_e32 v75, v22, v75
	v_exp_f32_e32 v22, v27
	v_exp_f32_e32 v23, v31
	v_mfma_f32_32x32x16_bf16 v[2:17], v[66:69], v[166:169], v[2:17]
	v_fmac_f32_e32 v70, v26, v70
	v_fmac_f32_e32 v71, v30, v71
	v_mov_b32_e32 v27, 0xc038aa3b
	v_add_f32_e32 v19, 1.0, v19
	v_rcp_f32_e32 v26, v74
	v_rcp_f32_e32 v30, v75
	v_rcp_f32_e32 v31, v70
	v_rcp_f32_e32 v66, v71
	v_mfma_f32_32x32x16_bf16 v[2:17], v[62:65], v[162:165], v[2:17]
	v_fmamk_f32 v20, v20, 0x4038aa3b, v27
	v_add_f32_e32 v18, 1.0, v18
	v_fmamk_f32 v24, v24, 0x4038aa3b, v27
	v_add_f32_e32 v22, 1.0, v22
	v_fmamk_f32 v28, v28, 0x4038aa3b, v27
	v_rcp_f32_e32 v19, v19
	v_rcp_f32_e32 v18, v18
	v_exp_f32_e32 v21, v21
	v_exp_f32_e32 v25, v25
	v_mfma_f32_32x32x16_bf16 v[2:17], v[58:61], v[158:161], v[2:17]
	v_add_f32_e32 v23, 1.0, v23
	v_fmamk_f32 v32, v32, 0x4038aa3b, v27
	v_mul_f32_e32 v20, v20, v26
	v_mul_f32_e32 v24, v24, v30
	v_rcp_f32_e32 v22, v22
	v_rcp_f32_e32 v23, v23
	v_exp_f32_e32 v26, v29
	v_exp_f32_e32 v29, v33
	v_mfma_f32_32x32x16_bf16 v[2:17], v[54:57], v[154:157], v[2:17]
	v_mul_f32_e32 v28, v28, v31
	v_mul_f32_e32 v30, v32, v66
	v_fmac_f32_e32 v20, v19, v201
	v_fmac_f32_e32 v24, v18, v200
	v_fmac_f32_e32 v28, v22, v199
	v_fmac_f32_e32 v30, v23, v198
	v_mfma_f32_32x32x16_bf16 v[2:17], v[50:53], v[142:145], v[2:17]
	v_add_f32_e32 v18, 1.0, v21
	v_exp_f32_e32 v19, v20
	v_add_f32_e32 v20, 1.0, v25
	v_exp_f32_e32 v21, v24
	v_exp_f32_e32 v22, v28
	v_exp_f32_e32 v23, v30
	v_mfma_f32_32x32x16_bf16 v[2:17], v[46:49], v[130:133], v[2:17]
	v_add_f32_e32 v24, 1.0, v26
	v_add_f32_e32 v25, 1.0, v29
	v_fmac_f32_e32 v18, v18, v19
	v_fmac_f32_e32 v20, v20, v21
	v_fmac_f32_e32 v24, v24, v22
	v_fmac_f32_e32 v25, v25, v23
	v_mfma_f32_32x32x16_bf16 v[2:17], v[42:45], v[134:137], v[2:17]
	v_rcp_f32_e32 v18, v18
	v_rcp_f32_e32 v20, v20
	v_rcp_f32_e32 v24, v24
	v_rcp_f32_e32 v25, v25
	v_mfma_f32_32x32x16_bf16 v[2:17], v[38:41], v[138:141], v[2:17]
	v_fma_f32 v18, -v19, v18, v18
	v_fma_f32 v19, -v21, v20, v20
	v_fma_f32 v20, -v22, v24, v24
	v_fma_f32 v21, -v23, v25, v25
	v_mfma_f32_32x32x16_bf16 v[2:17], v[34:37], v[146:149], v[2:17]
	v_cvt_pk_bf16_f32 v252, v18, v19
	v_cvt_pk_bf16_f32 v253, v20, v21
	s_nop 9
	v_exp_f32_e32 v4, v4
	v_exp_f32_e32 v8, v8
	v_exp_f32_e32 v12, v12
	v_exp_f32_e32 v16, v16
	v_exp_f32_e32 v2, v2
	v_add_f32_e32 v18, 1.0, v4
	v_exp_f32_e32 v6, v6
	v_exp_f32_e32 v10, v10
	v_exp_f32_e32 v14, v14
	v_add_f32_e32 v19, 1.0, v8
	v_add_f32_e32 v20, 1.0, v12
	v_add_f32_e32 v21, 1.0, v16
	v_exp_f32_e32 v3, v3
	v_fmac_f32_e32 v18, v2, v18
	v_exp_f32_e32 v2, v7
	v_exp_f32_e32 v7, v11
	v_exp_f32_e32 v11, v15
	v_fmac_f32_e32 v19, v6, v19
	v_fmac_f32_e32 v20, v10, v20
	v_fmac_f32_e32 v21, v14, v21
	v_add_f32_e32 v3, 1.0, v3
	v_rcp_f32_e32 v6, v18
	v_rcp_f32_e32 v10, v19
	v_rcp_f32_e32 v14, v20
	v_rcp_f32_e32 v15, v21
	v_fmamk_f32 v4, v4, 0x4038aa3b, v27
	v_add_f32_e32 v2, 1.0, v2
	v_fmamk_f32 v8, v8, 0x4038aa3b, v27
	v_add_f32_e32 v7, 1.0, v7
	v_rcp_f32_e32 v3, v3
	v_rcp_f32_e32 v2, v2
	v_exp_f32_e32 v5, v5
	v_exp_f32_e32 v9, v9
	v_fmamk_f32 v12, v12, 0x4038aa3b, v27
	v_add_f32_e32 v11, 1.0, v11
	v_fmac_f32_e32 v27, 0x4038aa3b, v16
	v_mul_f32_e32 v4, v4, v6
	v_rcp_f32_e32 v6, v7
	v_rcp_f32_e32 v7, v11
	v_exp_f32_e32 v11, v13
	v_exp_f32_e32 v13, v17
	v_mul_f32_e32 v8, v8, v10
	v_mul_f32_e32 v10, v12, v14
	v_mul_f32_e32 v12, v27, v15
	v_fmac_f32_e32 v4, v3, v207
	v_fmac_f32_e32 v8, v2, v206
	v_fmac_f32_e32 v10, v6, v209
	v_fmac_f32_e32 v12, v7, v208
	v_add_f32_e32 v2, 1.0, v5
	v_exp_f32_e32 v3, v4
	v_exp_f32_e32 v4, v8
	v_exp_f32_e32 v5, v10
	v_exp_f32_e32 v6, v12
	v_add_f32_e32 v7, 1.0, v9
	v_add_f32_e32 v8, 1.0, v11
	v_add_f32_e32 v9, 1.0, v13
	v_fmac_f32_e32 v2, v2, v3
	v_fmac_f32_e32 v7, v7, v4
	v_fmac_f32_e32 v8, v8, v5
	v_fmac_f32_e32 v9, v9, v6
	v_rcp_f32_e32 v2, v2
	v_rcp_f32_e32 v7, v7
	v_rcp_f32_e32 v8, v8
	v_rcp_f32_e32 v9, v9
	v_fma_f32 v2, -v3, v2, v2
	v_fma_f32 v3, -v4, v7, v7
	v_fma_f32 v4, -v5, v8, v8
	v_fma_f32 v5, -v6, v9, v9
	v_cvt_pk_bf16_f32 v254, v2, v3
	v_cvt_pk_bf16_f32 v255, v4, v5
	ds_write_b128 v211, v[252:255] offset:8192
	s_waitcnt lgkmcnt(0)
	s_barrier
